# v7 plus leaner DSA fast path: single wait per gather-index group, bf16 output packing by v_cvt_pk_bf16_f32
# speedup vs baseline: 1.0038x; 1.0018x over previous
.Lmy_dsa_fast_nk_skip:
	v_lshl_add_u32 v151, v247, 1, s19
	ds_read_u16 v46, v151
	ds_read_u16 v47, v151 offset:16
	ds_read_u16 v126, v151 offset:32
	ds_read_u16 v127, v151 offset:48
	s_waitcnt lgkmcnt(0)
	v_lshl_or_b32 v46, v46, 8, v250
	v_lshl_or_b32 v47, v47, 8, v250
	global_load_dwordx4 v[102:105], v46, s[50:51] offset:128
	global_load_dwordx4 v[110:113], v47, s[50:51] offset:128
	v_lshl_or_b32 v46, v126, 8, v250
	v_lshl_or_b32 v47, v127, 8, v250
	global_load_dwordx4 v[126:129], v46, s[50:51] offset:128
	global_load_dwordx4 v[130:133], v47, s[50:51] offset:128
	ds_read_u16 v46, v151 offset:64
	ds_read_u16 v47, v151 offset:80
	ds_read_u16 v118, v151 offset:96
	ds_read_u16 v119, v151 offset:112
	s_waitcnt lgkmcnt(0)
	v_lshl_or_b32 v46, v46, 8, v250
	v_lshl_or_b32 v47, v47, 8, v250
	global_load_dwordx4 v[86:89], v46, s[50:51] offset:128
	global_load_dwordx4 v[94:97], v47, s[50:51] offset:128
	v_lshl_or_b32 v46, v118, 8, v250
	v_lshl_or_b32 v47, v119, 8, v250
	global_load_dwordx4 v[118:121], v46, s[50:51] offset:128
	global_load_dwordx4 v[122:125], v47, s[50:51] offset:128
	ds_read_u16 v46, v151 offset:128
	ds_read_u16 v47, v151 offset:144
	ds_read_u16 v106, v151 offset:160
	ds_read_u16 v107, v151 offset:176
	s_waitcnt lgkmcnt(0)
	v_lshl_or_b32 v46, v46, 8, v250
	v_lshl_or_b32 v47, v47, 8, v250
	global_load_dwordx4 v[78:81], v46, s[50:51] offset:128
	global_load_dwordx4 v[82:85], v47, s[50:51] offset:128
	v_lshl_or_b32 v46, v106, 8, v250
	v_lshl_or_b32 v47, v107, 8, v250
	global_load_dwordx4 v[106:109], v46, s[50:51] offset:128
	global_load_dwordx4 v[114:117], v47, s[50:51] offset:128
	ds_read_u16 v46, v151 offset:192
	ds_read_u16 v47, v151 offset:208
	ds_read_u16 v90, v151 offset:224
	ds_read_u16 v91, v151 offset:240
	s_waitcnt lgkmcnt(0)
	v_lshl_or_b32 v46, v46, 8, v250
	v_lshl_or_b32 v47, v47, 8, v250
	global_load_dwordx4 v[70:73], v46, s[50:51] offset:128
	global_load_dwordx4 v[74:77], v47, s[50:51] offset:128
	v_lshl_or_b32 v46, v90, 8, v250
	v_lshl_or_b32 v47, v91, 8, v250
	global_load_dwordx4 v[90:93], v46, s[50:51] offset:128
	global_load_dwordx4 v[98:101], v47, s[50:51] offset:128
	v_mov_b32_e32 v46, v49
	s_nop 1
	v_permlane32_swap_b32 v49, v46
	s_nop 1
	s_nop 0
	v_max_f32_e32 v46, v46, v46
	v_max_f32_e32 v47, v49, v49
	v_max_f32_e32 v46, v47, v46
	v_mov_b32_e32 v47, v46
	s_nop 1
	v_permlane16_swap_b32 v46, v47
	s_nop 1
	s_nop 0
	v_max_f32_e32 v47, v47, v47
	v_max_f32_e32 v46, v46, v46
	v_max_f32_e32 v49, v46, v47
	s_mov_b32 s32, 0x3fb8aa3b
	v_mul_f32_e32 v49, 0xbfb8aa3b, v49
	v_fma_f32 v135, v141, s32, v49
	v_fma_f32 v141, v158, s32, v49
	v_exp_f32_e32 v226, v141
	v_fma_f32 v141, v159, s32, v49
	v_exp_f32_e32 v227, v141
	v_fma_f32 v141, v156, s32, v49
	v_exp_f32_e32 v228, v141
	v_fma_f32 v141, v157, s32, v49
	v_exp_f32_e32 v229, v141
	v_fma_f32 v141, v160, s32, v49
	v_exp_f32_e32 v230, v141
	v_fma_f32 v141, v161, s32, v49
	v_exp_f32_e32 v231, v141
	v_fma_f32 v141, v154, s32, v49
	v_exp_f32_e32 v232, v141
	v_fma_f32 v141, v155, s32, v49
	v_exp_f32_e32 v233, v141
	v_fma_f32 v141, v166, s32, v49
	v_exp_f32_e32 v218, v141
	v_fma_f32 v141, v167, s32, v49
	v_exp_f32_e32 v219, v141
	v_fma_f32 v141, v164, s32, v49
	v_exp_f32_e32 v220, v141
	v_fma_f32 v141, v165, s32, v49
	v_exp_f32_e32 v221, v141
	v_fma_f32 v141, v168, s32, v49
	v_exp_f32_e32 v222, v141
	v_fma_f32 v141, v169, s32, v49
	v_exp_f32_e32 v223, v141
	v_fma_f32 v141, v162, s32, v49
	v_exp_f32_e32 v224, v141
	v_fma_f32 v141, v163, s32, v49
	v_exp_f32_e32 v225, v141
	v_fma_f32 v141, v174, s32, v49
	v_exp_f32_e32 v206, v141
	v_fma_f32 v141, v175, s32, v49
	v_exp_f32_e32 v207, v141
	v_fma_f32 v141, v172, s32, v49
	v_fma_f32 v46, v142, s32, v49
	v_exp_f32_e32 v208, v141
	v_fma_f32 v141, v173, s32, v49
	v_fma_f32 v47, v143, s32, v49
	v_exp_f32_e32 v46, v46
	v_fma_f32 v134, v140, s32, v49
	v_exp_f32_e32 v209, v141
	v_fma_f32 v141, v176, s32, v49
	v_exp_f32_e32 v47, v47
	v_exp_f32_e32 v134, v134
	v_exp_f32_e32 v214, v141
	v_fma_f32 v141, v177, s32, v49
	v_exp_f32_e32 v135, v135
	v_add_f32_e32 v136, 0, v46
	v_exp_f32_e32 v215, v141
	v_fma_f32 v141, v170, s32, v49
	v_add_f32_e32 v136, v47, v136
	v_add_f32_e32 v136, v134, v136
	v_exp_f32_e32 v216, v141
	v_fma_f32 v141, v171, s32, v49
	v_add_f32_e32 v140, v135, v136
	v_fma_f32 v136, v144, s32, v49
	v_fma_f32 v137, v145, s32, v49
	v_exp_f32_e32 v217, v141
	v_fma_f32 v141, v182, s32, v49
	v_exp_f32_e32 v136, v136
	v_fma_f32 v138, v138, s32, v49
	v_exp_f32_e32 v137, v137
	v_fma_f32 v139, v139, s32, v49
	v_exp_f32_e32 v182, v141
	v_fma_f32 v141, v183, s32, v49
	v_exp_f32_e32 v138, v138
	v_exp_f32_e32 v139, v139
	v_exp_f32_e32 v183, v141
	v_fma_f32 v141, v180, s32, v49
	v_add_f32_e32 v140, v136, v140
	v_add_f32_e32 v140, v137, v140
	v_exp_f32_e32 v180, v141
	v_fma_f32 v141, v181, s32, v49
	v_add_f32_e32 v140, v138, v140
	v_add_f32_e32 v140, v139, v140
	v_exp_f32_e32 v181, v141
	v_fma_f32 v141, v184, s32, v49
	v_add_f32_e32 v140, v226, v140
	v_add_f32_e32 v140, v227, v140
	v_exp_f32_e32 v184, v141
	v_fma_f32 v141, v185, s32, v49
	v_add_f32_e32 v140, v228, v140
	v_add_f32_e32 v140, v229, v140
	v_exp_f32_e32 v185, v141
	v_fma_f32 v141, v178, s32, v49
	v_add_f32_e32 v140, v230, v140
	v_add_f32_e32 v140, v231, v140
	v_exp_f32_e32 v196, v141
	v_fma_f32 v141, v179, s32, v49
	v_add_f32_e32 v140, v232, v140
	v_add_f32_e32 v140, v233, v140
	v_exp_f32_e32 v197, v141
	v_fma_f32 v141, v190, s32, v49
	v_add_f32_e32 v140, v218, v140
	v_add_f32_e32 v140, v219, v140
	v_exp_f32_e32 v172, v141
	v_fma_f32 v141, v191, s32, v49
	v_add_f32_e32 v140, v220, v140
	v_add_f32_e32 v140, v221, v140
	v_exp_f32_e32 v173, v141
	v_fma_f32 v141, v188, s32, v49
	v_add_f32_e32 v140, v222, v140
	v_add_f32_e32 v140, v223, v140
	v_exp_f32_e32 v174, v141
	v_fma_f32 v141, v189, s32, v49
	v_add_f32_e32 v140, v224, v140
	v_add_f32_e32 v140, v225, v140
	v_exp_f32_e32 v175, v141
	v_fma_f32 v141, v192, s32, v49
	v_add_f32_e32 v140, v206, v140
	v_add_f32_e32 v140, v207, v140
	v_exp_f32_e32 v176, v141
	v_fma_f32 v141, v193, s32, v49
	v_add_f32_e32 v140, v208, v140
	v_add_f32_e32 v140, v209, v140
	v_exp_f32_e32 v177, v141
	v_fma_f32 v141, v186, s32, v49
	v_add_f32_e32 v140, v214, v140
	v_add_f32_e32 v140, v215, v140
	v_exp_f32_e32 v178, v141
	v_fma_f32 v141, v187, s32, v49
	v_add_f32_e32 v140, v216, v140
	v_add_f32_e32 v140, v217, v140
	v_exp_f32_e32 v179, v141
	v_fma_f32 v141, v200, s32, v49
	v_add_f32_e32 v140, v182, v140
	v_add_f32_e32 v140, v183, v140
	v_exp_f32_e32 v164, v141
	v_fma_f32 v141, v201, s32, v49
	v_add_f32_e32 v140, v180, v140
	v_add_f32_e32 v140, v181, v140
	v_exp_f32_e32 v165, v141
	v_fma_f32 v141, v198, s32, v49
	v_add_f32_e32 v140, v184, v140
	v_add_f32_e32 v140, v185, v140
	v_exp_f32_e32 v166, v141
	v_fma_f32 v141, v199, s32, v49
	v_add_f32_e32 v140, v196, v140
	v_add_f32_e32 v140, v197, v140
	v_exp_f32_e32 v167, v141
	v_fma_f32 v141, v202, s32, v49
	v_add_f32_e32 v140, v172, v140
	v_add_f32_e32 v140, v173, v140
	v_exp_f32_e32 v168, v141
	v_fma_f32 v141, v203, s32, v49
	v_add_f32_e32 v140, v174, v140
	v_add_f32_e32 v140, v175, v140
	v_exp_f32_e32 v169, v141
	v_fma_f32 v141, v194, s32, v49
	v_add_f32_e32 v140, v176, v140
	v_add_f32_e32 v140, v177, v140
	v_exp_f32_e32 v170, v141
	v_fma_f32 v141, v195, s32, v49
	v_add_f32_e32 v140, v178, v140
	v_add_f32_e32 v140, v179, v140
	v_exp_f32_e32 v171, v141
	v_fma_f32 v141, v212, s32, v49
	v_add_f32_e32 v140, v164, v140
	v_add_f32_e32 v140, v165, v140
	v_exp_f32_e32 v154, v141
	v_fma_f32 v141, v213, s32, v49
	v_add_f32_e32 v140, v166, v140
	v_add_f32_e32 v140, v167, v140
	v_exp_f32_e32 v155, v141
	v_fma_f32 v141, v210, s32, v49
	v_fma_f32 v44, v44, s32, v49
	v_add_f32_e32 v140, v168, v140
	v_add_f32_e32 v140, v169, v140
	v_exp_f32_e32 v156, v141
	v_fma_f32 v141, v211, s32, v49
	v_exp_f32_e32 v158, v44
	v_fma_f32 v44, v45, s32, v49
	v_add_f32_e32 v140, v170, v140
	v_add_f32_e32 v140, v171, v140
	v_exp_f32_e32 v157, v141
	v_exp_f32_e32 v159, v44
	v_fma_f32 v44, v204, s32, v49
	v_add_f32_e32 v140, v154, v140
	v_add_f32_e32 v140, v155, v140
	v_exp_f32_e32 v160, v44
	v_fma_f32 v44, v205, s32, v49
	v_add_f32_e32 v140, v156, v140
	v_add_f32_e32 v140, v157, v140
	v_exp_f32_e32 v161, v44
	v_add_f32_e32 v44, v158, v140
	v_add_f32_e32 v44, v159, v44
	v_add_f32_e32 v44, v160, v44
	v_add_f32_e32 v44, v161, v44
	v_mov_b32_e32 v45, v44
	s_nop 1
	v_permlane32_swap_b32 v44, v45
	s_nop 1
	s_nop 0
	v_add_f32_e32 v44, v44, v45
	v_mov_b32_e32 v45, v44
	s_nop 1
	v_permlane16_swap_b32 v44, v45
	s_nop 1
	s_nop 0
	v_add_f32_e32 v44, v44, v45
	v_div_scale_f32 v45, s[20:21], v44, v44, 1.0
	v_rcp_f32_e32 v49, v45
	s_nop 0
	v_fma_f32 v140, -v45, v49, 1.0
	v_fmac_f32_e32 v49, v140, v49
	v_div_scale_f32 v140, vcc, 1.0, v44, 1.0
	v_mul_f32_e32 v141, v140, v49
	v_fma_f32 v142, -v45, v141, v140
	v_fmac_f32_e32 v141, v142, v49
	v_fma_f32 v45, -v45, v141, v140
	v_div_fmas_f32 v45, v45, v49, v141
	v_div_fixup_f32 v162, v45, v44, 1.0
	s_waitcnt vmcnt(15)
	ds_write_b128 v252, v[102:105]
	s_waitcnt vmcnt(14)
	ds_write_b128 v252, v[110:113] offset:1152
	s_waitcnt vmcnt(13)
	ds_write_b128 v252, v[126:129] offset:2304
	s_waitcnt vmcnt(12)
	ds_write_b128 v252, v[130:133] offset:3456
	ds_read_u16 v44, v151 offset:256
	ds_read_u16 v45, v151 offset:272
	ds_read_u16 v49, v151 offset:288
	ds_read_u16 v126, v151 offset:304
	s_waitcnt lgkmcnt(0)
	v_lshl_or_b32 v44, v44, 8, v250
	v_lshl_or_b32 v45, v45, 8, v250
	global_load_dwordx4 v[102:105], v44, s[50:51] offset:128
	global_load_dwordx4 v[110:113], v45, s[50:51] offset:128
	v_lshl_or_b32 v44, v49, 8, v250
	v_lshl_or_b32 v45, v126, 8, v250
	global_load_dwordx4 v[126:129], v44, s[50:51] offset:128
	global_load_dwordx4 v[130:133], v45, s[50:51] offset:128
	v_pk_mul_f32 v[44:45], v[162:163], v[46:47] op_sel_hi:[0,1]
	v_pk_mul_f32 v[46:47], v[162:163], v[134:135] op_sel_hi:[0,1]
	v_cvt_pk_bf16_f32 v44, v44, v45
	v_cvt_pk_bf16_f32 v45, v46, v47
	v_pk_mul_f32 v[46:47], v[162:163], v[136:137] op_sel_hi:[0,1]
	v_pk_mul_f32 v[134:135], v[162:163], v[138:139] op_sel_hi:[0,1]
	s_waitcnt lgkmcnt(0)
	v_cvt_pk_bf16_f32 v46, v46, v47
	v_cvt_pk_bf16_f32 v47, v134, v135
	ds_read_b64_tr_b16 v[136:137], v249 offset:2304
	ds_read_b64_tr_b16 v[134:135], v249
	ds_read_b64_tr_b16 v[138:139], v249 offset:32
	ds_read_b64_tr_b16 v[186:187], v249 offset:64
	ds_read_b64_tr_b16 v[190:191], v249 offset:96
	ds_read_b64_tr_b16 v[140:141], v249 offset:2336
	ds_read_b64_tr_b16 v[188:189], v249 offset:2368
	ds_read_b64_tr_b16 v[192:193], v249 offset:2400
	s_waitcnt lgkmcnt(6)
	v_mfma_f32_16x16x32_bf16 v[142:145], v[44:47], v[134:137], 0
	s_waitcnt lgkmcnt(2)
	v_mfma_f32_16x16x32_bf16 v[138:141], v[44:47], v[138:141], 0
	s_waitcnt lgkmcnt(1)
	v_mfma_f32_16x16x32_bf16 v[134:137], v[44:47], v[186:189], 0
	s_waitcnt lgkmcnt(0)
	v_mfma_f32_16x16x32_bf16 v[44:47], v[44:47], v[190:193], 0
	s_waitcnt vmcnt(15)
	ds_write_b128 v252, v[86:89] offset:4608
	s_waitcnt vmcnt(14)
	ds_write_b128 v252, v[94:97] offset:5760
	s_waitcnt vmcnt(13)
	ds_write_b128 v252, v[118:121] offset:6912
	s_waitcnt vmcnt(12)
	ds_write_b128 v252, v[122:125] offset:8064
	ds_read_u16 v49, v151 offset:320
	ds_read_u16 v86, v151 offset:336
	ds_read_u16 v118, v151 offset:352
	ds_read_u16 v119, v151 offset:368
	s_waitcnt lgkmcnt(0)
	v_lshl_or_b32 v49, v49, 8, v250
	v_lshl_or_b32 v94, v86, 8, v250
	global_load_dwordx4 v[86:89], v49, s[50:51] offset:128
	s_nop 0
	global_load_dwordx4 v[94:97], v94, s[50:51] offset:128
	v_lshl_or_b32 v49, v118, 8, v250
	v_lshl_or_b32 v122, v119, 8, v250
	global_load_dwordx4 v[118:121], v49, s[50:51] offset:128
	s_nop 0
	global_load_dwordx4 v[122:125], v122, s[50:51] offset:128
	v_pk_mul_f32 v[186:187], v[162:163], v[226:227] op_sel_hi:[0,1]
	v_pk_mul_f32 v[188:189], v[162:163], v[228:229] op_sel_hi:[0,1]
	v_cvt_pk_bf16_f32 v186, v186, v187
	v_cvt_pk_bf16_f32 v187, v188, v189
	v_pk_mul_f32 v[188:189], v[162:163], v[230:231] op_sel_hi:[0,1]
	v_pk_mul_f32 v[190:191], v[162:163], v[232:233] op_sel_hi:[0,1]
	v_cvt_pk_bf16_f32 v188, v188, v189
	v_cvt_pk_bf16_f32 v189, v190, v191
	s_waitcnt lgkmcnt(0)
	ds_read_b64_tr_b16 v[192:193], v249 offset:6912
	ds_read_b64_tr_b16 v[190:191], v249 offset:4608
	ds_read_b64_tr_b16 v[198:199], v249 offset:4640
	s_waitcnt lgkmcnt(1)
	v_mfma_f32_16x16x32_bf16 v[142:145], v[186:189], v[190:193], v[142:145]
	ds_read_b64_tr_b16 v[200:201], v249 offset:6944
	ds_read_b64_tr_b16 v[190:191], v249 offset:4672
	ds_read_b64_tr_b16 v[192:193], v249 offset:6976
	s_waitcnt lgkmcnt(0)
	v_mfma_f32_16x16x32_bf16 v[134:137], v[186:189], v[190:193], v[134:137]
	ds_read_b64_tr_b16 v[190:191], v249 offset:4704
	ds_read_b64_tr_b16 v[192:193], v249 offset:7008
	v_mfma_f32_16x16x32_bf16 v[138:141], v[186:189], v[198:201], v[138:141]
	s_waitcnt lgkmcnt(0)
	v_mfma_f32_16x16x32_bf16 v[44:47], v[186:189], v[190:193], v[44:47]
	s_waitcnt vmcnt(15)
	ds_write_b128 v252, v[78:81]
	s_waitcnt vmcnt(14)
	ds_write_b128 v252, v[82:85] offset:1152
	s_waitcnt vmcnt(13)
	ds_write_b128 v252, v[106:109] offset:2304
	s_waitcnt vmcnt(12)
	ds_write_b128 v252, v[114:117] offset:3456
	ds_read_u16 v49, v151 offset:384
	ds_read_u16 v78, v151 offset:400
	ds_read_u16 v106, v151 offset:416
	ds_read_u16 v107, v151 offset:432
	s_waitcnt lgkmcnt(0)
	v_lshl_or_b32 v49, v49, 8, v250
	v_lshl_or_b32 v82, v78, 8, v250
	global_load_dwordx4 v[78:81], v49, s[50:51] offset:128
	s_nop 0
	global_load_dwordx4 v[82:85], v82, s[50:51] offset:128
	v_lshl_or_b32 v49, v106, 8, v250
	v_lshl_or_b32 v114, v107, 8, v250
	global_load_dwordx4 v[106:109], v49, s[50:51] offset:128
	s_nop 0
	global_load_dwordx4 v[114:117], v114, s[50:51] offset:128
	v_pk_mul_f32 v[186:187], v[162:163], v[218:219] op_sel_hi:[0,1]
	v_pk_mul_f32 v[188:189], v[162:163], v[220:221] op_sel_hi:[0,1]
	v_cvt_pk_bf16_f32 v186, v186, v187
	v_cvt_pk_bf16_f32 v187, v188, v189
	v_pk_mul_f32 v[188:189], v[162:163], v[222:223] op_sel_hi:[0,1]
	v_pk_mul_f32 v[190:191], v[162:163], v[224:225] op_sel_hi:[0,1]
	v_cvt_pk_bf16_f32 v188, v188, v189
	v_cvt_pk_bf16_f32 v189, v190, v191
	s_waitcnt lgkmcnt(0)
	ds_read_b64_tr_b16 v[192:193], v249 offset:2304
	ds_read_b64_tr_b16 v[190:191], v249
	ds_read_b64_tr_b16 v[198:199], v249 offset:32
	s_waitcnt lgkmcnt(1)
	v_mfma_f32_16x16x32_bf16 v[142:145], v[186:189], v[190:193], v[142:145]
	ds_read_b64_tr_b16 v[200:201], v249 offset:2336
	ds_read_b64_tr_b16 v[190:191], v249 offset:64
	ds_read_b64_tr_b16 v[192:193], v249 offset:2368
	s_waitcnt lgkmcnt(0)
	v_mfma_f32_16x16x32_bf16 v[134:137], v[186:189], v[190:193], v[134:137]
	ds_read_b64_tr_b16 v[190:191], v249 offset:96
	ds_read_b64_tr_b16 v[192:193], v249 offset:2400
	v_mfma_f32_16x16x32_bf16 v[138:141], v[186:189], v[198:201], v[138:141]
	s_waitcnt lgkmcnt(0)
	v_mfma_f32_16x16x32_bf16 v[44:47], v[186:189], v[190:193], v[44:47]
	s_waitcnt vmcnt(15)
	ds_write_b128 v252, v[70:73] offset:4608
	s_waitcnt vmcnt(14)
	ds_write_b128 v252, v[74:77] offset:5760
	s_waitcnt vmcnt(13)
	ds_write_b128 v252, v[90:93] offset:6912
	s_waitcnt vmcnt(12)
	ds_write_b128 v252, v[98:101] offset:8064
	ds_read_u16 v49, v151 offset:448
	ds_read_u16 v70, v151 offset:464
	ds_read_u16 v90, v151 offset:480
	ds_read_u16 v91, v151 offset:496
	s_waitcnt lgkmcnt(0)
	v_lshl_or_b32 v49, v49, 8, v250
	v_lshl_or_b32 v74, v70, 8, v250
	global_load_dwordx4 v[70:73], v49, s[50:51] offset:128
	s_nop 0
	global_load_dwordx4 v[74:77], v74, s[50:51] offset:128
	v_lshl_or_b32 v49, v90, 8, v250
	v_lshl_or_b32 v98, v91, 8, v250
	global_load_dwordx4 v[90:93], v49, s[50:51] offset:128
	s_nop 0
	global_load_dwordx4 v[98:101], v98, s[50:51] offset:128
	v_pk_mul_f32 v[186:187], v[162:163], v[206:207] op_sel_hi:[0,1]
	v_pk_mul_f32 v[188:189], v[162:163], v[208:209] op_sel_hi:[0,1]
	v_cvt_pk_bf16_f32 v186, v186, v187
	v_cvt_pk_bf16_f32 v187, v188, v189
	v_pk_mul_f32 v[188:189], v[162:163], v[214:215] op_sel_hi:[0,1]
	v_pk_mul_f32 v[190:191], v[162:163], v[216:217] op_sel_hi:[0,1]
	v_cvt_pk_bf16_f32 v188, v188, v189
	v_cvt_pk_bf16_f32 v189, v190, v191
	s_waitcnt lgkmcnt(0)
	ds_read_b64_tr_b16 v[192:193], v249 offset:6912
	ds_read_b64_tr_b16 v[190:191], v249 offset:4608
	ds_read_b64_tr_b16 v[198:199], v249 offset:4640
	s_waitcnt lgkmcnt(1)
	v_mfma_f32_16x16x32_bf16 v[142:145], v[186:189], v[190:193], v[142:145]
	ds_read_b64_tr_b16 v[200:201], v249 offset:6944
	ds_read_b64_tr_b16 v[190:191], v249 offset:4672
	ds_read_b64_tr_b16 v[192:193], v249 offset:6976
	s_waitcnt lgkmcnt(0)
	v_mfma_f32_16x16x32_bf16 v[134:137], v[186:189], v[190:193], v[134:137]
	ds_read_b64_tr_b16 v[190:191], v249 offset:4704
	ds_read_b64_tr_b16 v[192:193], v249 offset:7008
	v_mfma_f32_16x16x32_bf16 v[138:141], v[186:189], v[198:201], v[138:141]
	s_waitcnt lgkmcnt(0)
	v_mfma_f32_16x16x32_bf16 v[44:47], v[186:189], v[190:193], v[44:47]
	v_pk_mul_f32 v[182:183], v[162:163], v[182:183] op_sel_hi:[0,1]
	v_pk_mul_f32 v[180:181], v[162:163], v[180:181] op_sel_hi:[0,1]
	v_cvt_pk_bf16_f32 v182, v182, v183
	v_cvt_pk_bf16_f32 v183, v180, v181
	v_pk_mul_f32 v[180:181], v[162:163], v[184:185] op_sel_hi:[0,1]
	s_waitcnt vmcnt(15)
	ds_write_b128 v252, v[102:105]
	s_waitcnt vmcnt(14)
	ds_write_b128 v252, v[110:113] offset:1152
	s_waitcnt vmcnt(13)
	ds_write_b128 v252, v[126:129] offset:2304
	s_waitcnt vmcnt(12)
	ds_write_b128 v252, v[130:133] offset:3456
	v_cvt_pk_bf16_f32 v184, v180, v181
	v_pk_mul_f32 v[180:181], v[162:163], v[196:197] op_sel_hi:[0,1]
	v_cvt_pk_bf16_f32 v185, v180, v181
	s_waitcnt lgkmcnt(0)
	ds_read_b64_tr_b16 v[188:189], v249 offset:2304
	ds_read_b64_tr_b16 v[186:187], v249
	ds_read_b64_tr_b16 v[190:191], v249 offset:32
	s_waitcnt lgkmcnt(1)
	v_mfma_f32_16x16x32_bf16 v[142:145], v[182:185], v[186:189], v[142:145]
	ds_read_b64_tr_b16 v[192:193], v249 offset:2336
	ds_read_b64_tr_b16 v[186:187], v249 offset:64
	ds_read_b64_tr_b16 v[188:189], v249 offset:2368
	s_waitcnt lgkmcnt(0)
	v_mfma_f32_16x16x32_bf16 v[134:137], v[182:185], v[186:189], v[134:137]
	ds_read_b64_tr_b16 v[186:187], v249 offset:96
	ds_read_b64_tr_b16 v[188:189], v249 offset:2400
	v_mfma_f32_16x16x32_bf16 v[138:141], v[182:185], v[190:193], v[138:141]
	s_waitcnt lgkmcnt(0)
	v_mfma_f32_16x16x32_bf16 v[44:47], v[182:185], v[186:189], v[44:47]
	v_pk_mul_f32 v[172:173], v[162:163], v[172:173] op_sel_hi:[0,1]
	v_pk_mul_f32 v[174:175], v[162:163], v[174:175] op_sel_hi:[0,1]
	s_waitcnt vmcnt(11)
	ds_write_b128 v252, v[86:89] offset:4608
	s_waitcnt vmcnt(10)
	ds_write_b128 v252, v[94:97] offset:5760
	s_waitcnt vmcnt(9)
	ds_write_b128 v252, v[118:121] offset:6912
	s_waitcnt vmcnt(8)
	ds_write_b128 v252, v[122:125] offset:8064
	v_cvt_pk_bf16_f32 v172, v172, v173
	v_cvt_pk_bf16_f32 v173, v174, v175
	v_pk_mul_f32 v[174:175], v[162:163], v[176:177] op_sel_hi:[0,1]
	v_pk_mul_f32 v[176:177], v[162:163], v[178:179] op_sel_hi:[0,1]
	v_cvt_pk_bf16_f32 v174, v174, v175
	v_cvt_pk_bf16_f32 v175, v176, v177
	s_waitcnt lgkmcnt(0)
	ds_read_b64_tr_b16 v[178:179], v249 offset:6912
	ds_read_b64_tr_b16 v[176:177], v249 offset:4608
	ds_read_b64_tr_b16 v[180:181], v249 offset:4640
	s_waitcnt lgkmcnt(1)
	v_mfma_f32_16x16x32_bf16 v[142:145], v[172:175], v[176:179], v[142:145]
	ds_read_b64_tr_b16 v[182:183], v249 offset:6944
	ds_read_b64_tr_b16 v[176:177], v249 offset:4672
	ds_read_b64_tr_b16 v[178:179], v249 offset:6976
	s_waitcnt lgkmcnt(0)
	v_mfma_f32_16x16x32_bf16 v[134:137], v[172:175], v[176:179], v[134:137]
	ds_read_b64_tr_b16 v[176:177], v249 offset:4704
	ds_read_b64_tr_b16 v[178:179], v249 offset:7008
	v_mfma_f32_16x16x32_bf16 v[138:141], v[172:175], v[180:183], v[138:141]
	s_waitcnt lgkmcnt(0)
	v_mfma_f32_16x16x32_bf16 v[44:47], v[172:175], v[176:179], v[44:47]
	v_pk_mul_f32 v[164:165], v[162:163], v[164:165] op_sel_hi:[0,1]
	v_pk_mul_f32 v[166:167], v[162:163], v[166:167] op_sel_hi:[0,1]
	s_waitcnt vmcnt(7)
	ds_write_b128 v252, v[78:81]
	s_waitcnt vmcnt(6)
	ds_write_b128 v252, v[82:85] offset:1152
	s_waitcnt vmcnt(5)
	ds_write_b128 v252, v[106:109] offset:2304
	s_waitcnt vmcnt(4)
	ds_write_b128 v252, v[114:117] offset:3456
	v_cvt_pk_bf16_f32 v164, v164, v165
	v_cvt_pk_bf16_f32 v165, v166, v167
	v_pk_mul_f32 v[166:167], v[162:163], v[168:169] op_sel_hi:[0,1]
	v_pk_mul_f32 v[168:169], v[162:163], v[170:171] op_sel_hi:[0,1]
	v_cvt_pk_bf16_f32 v166, v166, v167
	v_cvt_pk_bf16_f32 v167, v168, v169
	s_waitcnt lgkmcnt(0)
	ds_read_b64_tr_b16 v[170:171], v249 offset:2304
	ds_read_b64_tr_b16 v[168:169], v249
	ds_read_b64_tr_b16 v[172:173], v249 offset:32
	s_waitcnt lgkmcnt(1)
	v_mfma_f32_16x16x32_bf16 v[142:145], v[164:167], v[168:171], v[142:145]
	ds_read_b64_tr_b16 v[174:175], v249 offset:2336
	ds_read_b64_tr_b16 v[168:169], v249 offset:64
	ds_read_b64_tr_b16 v[170:171], v249 offset:2368
	s_waitcnt lgkmcnt(0)
	v_mfma_f32_16x16x32_bf16 v[134:137], v[164:167], v[168:171], v[134:137]
	ds_read_b64_tr_b16 v[168:169], v249 offset:96
	ds_read_b64_tr_b16 v[170:171], v249 offset:2400
	v_mfma_f32_16x16x32_bf16 v[138:141], v[164:167], v[172:175], v[138:141]
	s_waitcnt lgkmcnt(0)
	v_mfma_f32_16x16x32_bf16 v[44:47], v[164:167], v[168:171], v[44:47]
	v_pk_mul_f32 v[154:155], v[162:163], v[154:155] op_sel_hi:[0,1]
	v_pk_mul_f32 v[156:157], v[162:163], v[156:157] op_sel_hi:[0,1]
	s_waitcnt vmcnt(3)
	ds_write_b128 v252, v[70:73] offset:4608
	s_waitcnt vmcnt(2)
	ds_write_b128 v252, v[74:77] offset:5760
	s_waitcnt vmcnt(1)
	ds_write_b128 v252, v[90:93] offset:6912
	s_waitcnt vmcnt(0)
	ds_write_b128 v252, v[98:101] offset:8064
	v_cvt_pk_bf16_f32 v154, v154, v155
	v_cvt_pk_bf16_f32 v155, v156, v157
	v_pk_mul_f32 v[156:157], v[162:163], v[158:159] op_sel_hi:[0,1]
	v_pk_mul_f32 v[158:159], v[162:163], v[160:161] op_sel_hi:[0,1]
	v_cvt_pk_bf16_f32 v156, v156, v157
	v_cvt_pk_bf16_f32 v157, v158, v159
	s_waitcnt lgkmcnt(0)
	ds_read_b64_tr_b16 v[160:161], v249 offset:6912
	ds_read_b64_tr_b16 v[158:159], v249 offset:4608
	ds_read_b64_tr_b16 v[162:163], v249 offset:4640
	s_waitcnt lgkmcnt(1)
	v_mfma_f32_16x16x32_bf16 v[142:145], v[154:157], v[158:161], v[142:145]
	ds_read_b64_tr_b16 v[164:165], v249 offset:6944
	ds_read_b64_tr_b16 v[158:159], v249 offset:4672
	ds_read_b64_tr_b16 v[160:161], v249 offset:6976
	s_waitcnt lgkmcnt(0)
	v_mfma_f32_16x16x32_bf16 v[134:137], v[154:157], v[158:161], v[134:137]
	ds_read_b64_tr_b16 v[158:159], v249 offset:4704
	ds_read_b64_tr_b16 v[160:161], v249 offset:7008
	v_mfma_f32_16x16x32_bf16 v[138:141], v[154:157], v[162:165], v[138:141]
	s_waitcnt lgkmcnt(0)
	v_mfma_f32_16x16x32_bf16 v[44:47], v[154:157], v[158:161], v[44:47]
	s_waitcnt lgkmcnt(0)
	s_and_saveexec_b64 s[8:9], s[40:41]
	s_cbranch_execz .LBB0_784
	s_lshl_b64 s[18:19], s[52:53], 10
	v_lshl_add_u64 v[154:155], v[148:149], 0, s[18:19]
	v_cvt_pk_bf16_f32 v49, v142, v143
	global_store_short v[154:155], v49, off
	global_store_short_d16_hi v[154:155], v49, off offset:128
	v_cvt_pk_bf16_f32 v49, v144, v145
	global_store_short v[154:155], v49, off offset:256
	global_store_short_d16_hi v[154:155], v49, off offset:384
	v_cvt_pk_bf16_f32 v49, v138, v139
	global_store_short v[154:155], v49, off offset:32
	global_store_short_d16_hi v[154:155], v49, off offset:160
	v_cvt_pk_bf16_f32 v49, v140, v141
	global_store_short v[154:155], v49, off offset:288
	global_store_short_d16_hi v[154:155], v49, off offset:416
	v_cvt_pk_bf16_f32 v49, v134, v135
	global_store_short v[154:155], v49, off offset:64
	global_store_short_d16_hi v[154:155], v49, off offset:192
	v_cvt_pk_bf16_f32 v49, v136, v137
	global_store_short v[154:155], v49, off offset:320
	global_store_short_d16_hi v[154:155], v49, off offset:448
	v_cvt_pk_bf16_f32 v49, v44, v45
	global_store_short v[154:155], v49, off offset:96
	global_store_short_d16_hi v[154:155], v49, off offset:224
	v_cvt_pk_bf16_f32 v49, v46, v47
	global_store_short v[154:155], v49, off offset:352
	global_store_short_d16_hi v[154:155], v49, off offset:480
	s_branch .LBB0_784
